# v50 + G3 epilogue two-stage rstd8: ai=0 rows' SS partial sums prefetched at unit top into spare VGPRs (no wait in epilogue), ai=1 rows' loaded at epilogue start and consumed after the first four row b
# speedup vs baseline: 1.0089x; 1.0089x over previous
; #define PG8_STAGE_A(b, h, ptr, NX) do { if constexpr (Sched::GATHER) { unsigned gs_[2]; gs_[0] = ((NX) && last_) ? gN[h][0] : gA[h][0]; gs_[1] = ((NX) && last_) ? gN[h][1] : gA[h][1]; PG8_STAGE(PG8_SA(b, h), ptr, gs_); } \
;         else PG8_STAGE(PG8_SA(b, h), (ptr) + ((h) ? hstep : (size_t)0), voffA); } while (0)
; #define PG8_STAGE(bufoff, gbase, voff) do { _Pragma("unroll") for (int _i = 0; _i < 2; ++_i) \
;         __builtin_amdgcn_global_load_lds((const unsigned*)((const char*)(gbase) + (voff)[_i]), (PG8_LAS unsigned*)(lds + (bufoff) + ldsw + _i * 8192), 16, 0, 0); } while (0)
; #define PG8_LDA(dst, b, h) do { _Pragma("unroll") for (int m = 0; m < 4; ++m) _Pragma("unroll") for (int k = 0; k < 2; ++k) dst[m][k] = *(const PG8_LAS bf16x8*)(lds + PG8_SA(b, h) + aoff + m * 2048 + k * 1024); } while (0)
; #define PG8_LDB(dst, b, h) do { _Pragma("unroll") for (int n = 0; n < 2; ++n) _Pragma("unroll") for (int k = 0; k < 2; ++k) dst[n][k] = *(const PG8_LAS bf16x8*)(lds + PG8_SB(b, h) + boff + n * 2048 + k * 1024); } while (0)
; #define PG8_WAIT_V(n) asm volatile("s_waitcnt vmcnt(" #n ")" ::: "memory")
; #define PG8_WAIT_L(n) asm volatile("s_waitcnt lgkmcnt(" #n ")" ::: "memory")
; #define PG8_BAR __builtin_amdgcn_s_barrier()
; #define PG8_SCHED __builtin_amdgcn_sched_barrier(0)
; __device__ __forceinline__ void rstd8(const float* SS, int rowb, int lane, float (&rs)[2][4]) {
;     f32x4 p[2][4];
; #pragma unroll
;     for (int ai = 0; ai < 2; ++ai)
; #pragma unroll
;         for (int m = 0; m < 4; ++m) p[ai][m] = *(const f32x4*)(SS + (size_t)(rowb + HALF * ai + 16 * m + (lane >> 2)) * 16 + 4 * (lane & 3));
; template <class Epi, class Sched, bool ALIGN_EPI = false, bool SP2 = false>
; __device__ __forceinline__ void gemm_phase(PG8_LAS unsigned char* lds, const Gemm g, const Sched& S, const Epi& E, const bool skip_epi = false) {
;     ...
;             PG8_LDB(B0, 0, 0); PG8_LDB(B1, 0, 1); PG8_SCHED; PG8_LDA(At, 0, 0); PG8_STAGE_A(1, 1, a1, false);
;             PG8_WAIT_V(8); PG8_WAIT_L(0); PG8_BAR; PG8_MMA(0, 0, At, B0); PG8_MMA(0, 1, At, B1); PG8_BAR; PG8_SCHED;
;             PG8_LDA(At, 0, 1); PG8_STAGE(PG8_SB(0, 0), b2, voffB); PG8_STAGE(PG8_SB(0, 1), b2 + hstep, voffB); PG8_STAGE_A(0, 0, a2, true);
;             PG8_WAIT_V(8); PG8_WAIT_L(0); PG8_BAR; PG8_MMA(1, 0, At, B0); PG8_MMA(1, 1, At, B1); PG8_BAR; PG8_SCHED;
.LBB0_720:
	s_ashr_i32 s15, s14, 31
	s_lshl_b64 s[16:17], s[14:15], 19
	s_add_u32 s16, s86, s16
	s_addc_u32 s17, s87, s17
	s_and_b64 s[18:19], s[4:5], exec
	s_cselect_b32 s15, s17, s23
	s_cselect_b32 s56, s16, s22
	s_ashr_i32 s13, s12, 31
	s_lshl_b64 s[18:19], s[12:13], 19
	v_readlane_b32 s26, v254, 15
	v_readlane_b32 s27, v254, 16
	s_add_u32 s18, s26, s18
	s_addc_u32 s19, s27, s19
	s_and_b64 s[26:27], s[4:5], exec
	s_cselect_b32 s13, s19, s25
	s_cselect_b32 s57, s18, s24
	s_add_u32 s22, s22, 0x40080
	s_addc_u32 s23, s23, 0
	s_add_u32 s58, s24, 0x100
	s_addc_u32 s59, s25, 0
	s_mov_b32 s60, -2
	s_waitcnt vmcnt(0)
	v_lshl_add_u32 v130, s20, 8, v175
	v_ashrrev_i32_e32 v131, 31, v130
	v_lshlrev_b64 v[130:131], 6, v[130:131]
	v_lshl_add_u64 v[130:131], v[150:151], 0, v[130:131]
	global_load_dwordx4 v[238:241], v[130:131], off
	global_load_dwordx4 v[242:245], v[130:131], off offset:1024
	global_load_dwordx4 v[246:249], v[130:131], off offset:2048
	global_load_dwordx4 v[250:253], v[130:131], off offset:3072
	ds_read_b128 v[130:133], v187
	ds_read_b128 v[134:137], v187 offset:1024
	ds_read_b128 v[138:141], v187 offset:2048
	ds_read_b128 v[160:163], v187 offset:3072
	ds_read_b128 v[164:167], v188
	ds_read_b128 v[182:185], v188 offset:1024
	ds_read_b128 v[192:195], v188 offset:2048
	ds_read_b128 v[196:199], v188 offset:3072
	s_add_u32 s24, s22, 0xfffc0080
	s_addc_u32 s25, s23, -1
	s_cmp_eq_u32 s60, 12
	s_cselect_b32 s27, s15, s25
	s_cselect_b32 s26, s56, s24
	s_cselect_b32 s25, s13, s59
	s_cselect_b32 s24, s57, s58
	v_lshl_add_u64 v[168:169], s[22:23], 0, v[152:153]
	s_add_i32 m0, s29, 0xc000
	ds_read_b128 v[200:203], v189
	ds_read_b128 v[204:207], v189 offset:1024
	ds_read_b128 v[208:211], v189 offset:2048
	ds_read_b128 v[212:215], v189 offset:3072
	ds_read_b128 v[216:219], v189 offset:4096
	ds_read_b128 v[220:223], v189 offset:5120
	ds_read_b128 v[224:227], v189 offset:6144
	ds_read_b128 v[230:233], v189 offset:7168
	global_load_lds_dwordx4 v[168:169], off
	v_lshl_add_u64 v[168:169], s[22:23], 0, v[154:155]
	s_add_i32 m0, s29, 0xe000
	s_nop 0
	global_load_lds_dwordx4 v[168:169], off
	s_waitcnt vmcnt(8)
	s_waitcnt lgkmcnt(0)
	s_barrier
	s_setprio 1
	s_waitcnt lgkmcnt(0)
	v_mfma_f32_16x16x32_bf16 v[126:129], v[130:133], v[200:203], 0
	v_mfma_f32_16x16x32_bf16 v[122:125], v[138:141], v[200:203], 0
	v_mfma_f32_16x16x32_bf16 v[110:113], v[130:133], v[208:211], 0
	v_mfma_f32_16x16x32_bf16 v[106:109], v[138:141], v[208:211], 0
	v_mfma_f32_16x16x32_bf16 v[94:97], v[130:133], v[216:219], 0
	v_mfma_f32_16x16x32_bf16 v[90:93], v[138:141], v[216:219], 0
	v_mfma_f32_16x16x32_bf16 v[78:81], v[130:133], v[224:227], 0
	v_mfma_f32_16x16x32_bf16 v[74:77], v[138:141], v[224:227], 0
	v_mfma_f32_16x16x32_bf16 v[126:129], v[134:137], v[204:207], v[126:129]
	v_mfma_f32_16x16x32_bf16 v[122:125], v[160:163], v[204:207], v[122:125]
	v_mfma_f32_16x16x32_bf16 v[110:113], v[134:137], v[212:215], v[110:113]
	v_mfma_f32_16x16x32_bf16 v[106:109], v[160:163], v[212:215], v[106:109]
	v_mfma_f32_16x16x32_bf16 v[94:97], v[134:137], v[220:223], v[94:97]
	v_mfma_f32_16x16x32_bf16 v[90:93], v[160:163], v[220:223], v[90:93]
	v_mfma_f32_16x16x32_bf16 v[78:81], v[134:137], v[230:233], v[78:81]
	v_mfma_f32_16x16x32_bf16 v[74:77], v[160:163], v[230:233], v[74:77]
	s_setprio 0
	s_setprio 1
	v_mfma_f32_16x16x32_bf16 v[118:121], v[164:167], v[200:203], 0
	v_mfma_f32_16x16x32_bf16 v[114:117], v[192:195], v[200:203], 0
	v_mfma_f32_16x16x32_bf16 v[102:105], v[164:167], v[208:211], 0
	v_mfma_f32_16x16x32_bf16 v[98:101], v[192:195], v[208:211], 0
	v_mfma_f32_16x16x32_bf16 v[86:89], v[164:167], v[216:219], 0
	v_mfma_f32_16x16x32_bf16 v[82:85], v[192:195], v[216:219], 0
	v_mfma_f32_16x16x32_bf16 v[70:73], v[164:167], v[224:227], 0
	v_mfma_f32_16x16x32_bf16 v[66:69], v[192:195], v[224:227], 0
	v_mfma_f32_16x16x32_bf16 v[118:121], v[182:185], v[204:207], v[118:121]
	v_mfma_f32_16x16x32_bf16 v[114:117], v[196:199], v[204:207], v[114:117]
	v_mfma_f32_16x16x32_bf16 v[102:105], v[182:185], v[212:215], v[102:105]
	v_mfma_f32_16x16x32_bf16 v[98:101], v[196:199], v[212:215], v[98:101]
	v_mfma_f32_16x16x32_bf16 v[86:89], v[182:185], v[220:223], v[86:89]
	v_mfma_f32_16x16x32_bf16 v[82:85], v[196:199], v[220:223], v[82:85]
	v_mfma_f32_16x16x32_bf16 v[70:73], v[182:185], v[230:233], v[70:73]
	v_mfma_f32_16x16x32_bf16 v[66:69], v[196:199], v[230:233], v[66:69]
	s_setprio 0
	s_barrier
	s_add_i32 s61, s39, s2
	v_lshl_add_u64 v[168:169], s[24:25], 0, v[146:147]
	s_mov_b32 m0, s61
	ds_read_b128 v[200:203], v189 offset:16384
	ds_read_b128 v[204:207], v189 offset:17408
	ds_read_b128 v[208:211], v189 offset:18432
	ds_read_b128 v[212:215], v189 offset:19456
	ds_read_b128 v[216:219], v189 offset:20480
	ds_read_b128 v[220:223], v189 offset:21504
	ds_read_b128 v[224:227], v189 offset:22528
	ds_read_b128 v[230:233], v189 offset:23552
	global_load_lds_dwordx4 v[168:169], off
	s_add_i32 m0, s61, 0x2000
	s_add_u32 s62, s24, 0x40000
	v_lshl_add_u64 v[172:173], s[24:25], 0, v[142:143]
	s_addc_u32 s63, s25, 0
	s_add_i32 s61, s48, s2
	global_load_lds_dwordx4 v[172:173], off
	v_lshl_add_u64 v[176:177], s[62:63], 0, v[146:147]
	s_mov_b32 m0, s61
	v_lshl_add_u64 v[234:235], s[26:27], 0, v[144:145]
	global_load_lds_dwordx4 v[176:177], off
	v_lshl_add_u64 v[176:177], s[62:63], 0, v[142:143]
	s_add_i32 m0, s61, 0x2000
	s_nop 0
	global_load_lds_dwordx4 v[176:177], off
	v_lshl_add_u64 v[176:177], s[26:27], 0, v[148:149]
	s_mov_b32 m0, s29
	s_nop 0
	global_load_lds_dwordx4 v[176:177], off
	s_mov_b32 m0, s30
	s_nop 0
	global_load_lds_dwordx4 v[234:235], off
	s_waitcnt vmcnt(8)
	s_waitcnt lgkmcnt(0)
	s_barrier
; #define PG8_STAGE_A(b, h, ptr, NX) do { if constexpr (Sched::GATHER) { unsigned gs_[2]; gs_[0] = ((NX) && last_) ? gN[h][0] : gA[h][0]; gs_[1] = ((NX) && last_) ? gN[h][1] : gA[h][1]; PG8_STAGE(PG8_SA(b, h), ptr, gs_); } \
;         else PG8_STAGE(PG8_SA(b, h), (ptr) + ((h) ? hstep : (size_t)0), voffA); } while (0)
; #define PG8_STAGE(bufoff, gbase, voff) do { _Pragma("unroll") for (int _i = 0; _i < 2; ++_i) \
;         __builtin_amdgcn_global_load_lds((const unsigned*)((const char*)(gbase) + (voff)[_i]), (PG8_LAS unsigned*)(lds + (bufoff) + ldsw + _i * 8192), 16, 0, 0); } while (0)
; #define PG8_LDA(dst, b, h) do { _Pragma("unroll") for (int m = 0; m < 4; ++m) _Pragma("unroll") for (int k = 0; k < 2; ++k) dst[m][k] = *(const PG8_LAS bf16x8*)(lds + PG8_SA(b, h) + aoff + m * 2048 + k * 1024); } while (0)
; #define PG8_LDB(dst, b, h) do { _Pragma("unroll") for (int n = 0; n < 2; ++n) _Pragma("unroll") for (int k = 0; k < 2; ++k) dst[n][k] = *(const PG8_LAS bf16x8*)(lds + PG8_SB(b, h) + boff + n * 2048 + k * 1024); } while (0)
; #define PG8_MMA(ai, bj, At, Bt) do { __builtin_amdgcn_s_setprio(1); _Pragma("unroll") for (int m = 0; m < 4; ++m) _Pragma("unroll") for (int n = 0; n < 2; ++n) _Pragma("unroll") for (int k = 0; k < 2; ++k) \
;         acc[ai][bj][m][n] = __builtin_amdgcn_mfma_f32_16x16x32_bf16(Bt[n][k], At[m][k], acc[ai][bj][m][n], 0, 0, 0); __builtin_amdgcn_s_setprio(0); } while (0)
; #define PG8_WAIT_V(n) asm volatile("s_waitcnt vmcnt(" #n ")" ::: "memory")
; #define PG8_WAIT_L(n) asm volatile("s_waitcnt lgkmcnt(" #n ")" ::: "memory")
; #define PG8_BAR __builtin_amdgcn_s_barrier()
; #define PG8_SCHED __builtin_amdgcn_sched_barrier(0)
; template <class Epi, class Sched, bool ALIGN_EPI = false, bool SP2 = false>
; __device__ __forceinline__ void gemm_phase(PG8_LAS unsigned char* lds, const Gemm g, const Sched& S, const Epi& E, const bool skip_epi = false) {
;     ...
;             PG8_WAIT_V(8); PG8_WAIT_L(0); PG8_BAR; PG8_MMA(1, 0, At, B0); PG8_MMA(1, 1, At, B1); PG8_BAR; PG8_SCHED;
;             PG8_LDB(B0, 1, 0); PG8_LDB(B1, 1, 1); PG8_SCHED; PG8_LDA(At, 1, 0); PG8_STAGE_A(0, 1, a2, true);
;             PG8_WAIT_V(8); PG8_WAIT_L(0); PG8_BAR; PG8_MMA(0, 0, At, B0); PG8_MMA(0, 1, At, B1); PG8_BAR; PG8_SCHED;
;             PG8_LDA(At, 1, 1); PG8_STAGE(PG8_SB(1, 0), b3, voffB); PG8_STAGE(PG8_SB(1, 1), b3 + hstep, voffB); PG8_STAGE_A(1, 0, a3, true);
	s_setprio 1
	s_waitcnt lgkmcnt(0)
	v_mfma_f32_16x16x32_bf16 v[62:65], v[130:133], v[200:203], 0
	v_mfma_f32_16x16x32_bf16 v[58:61], v[138:141], v[200:203], 0
	v_mfma_f32_16x16x32_bf16 v[46:49], v[130:133], v[208:211], 0
	v_mfma_f32_16x16x32_bf16 v[42:45], v[138:141], v[208:211], 0
	v_mfma_f32_16x16x32_bf16 v[30:33], v[130:133], v[216:219], 0
	v_mfma_f32_16x16x32_bf16 v[26:29], v[138:141], v[216:219], 0
	v_mfma_f32_16x16x32_bf16 v[14:17], v[130:133], v[224:227], 0
	v_mfma_f32_16x16x32_bf16 v[10:13], v[138:141], v[224:227], 0
	v_mfma_f32_16x16x32_bf16 v[62:65], v[134:137], v[204:207], v[62:65]
	v_mfma_f32_16x16x32_bf16 v[58:61], v[160:163], v[204:207], v[58:61]
	v_mfma_f32_16x16x32_bf16 v[46:49], v[134:137], v[212:215], v[46:49]
	v_mfma_f32_16x16x32_bf16 v[42:45], v[160:163], v[212:215], v[42:45]
	v_mfma_f32_16x16x32_bf16 v[30:33], v[134:137], v[220:223], v[30:33]
	v_mfma_f32_16x16x32_bf16 v[26:29], v[160:163], v[220:223], v[26:29]
	v_mfma_f32_16x16x32_bf16 v[14:17], v[134:137], v[230:233], v[14:17]
	v_mfma_f32_16x16x32_bf16 v[10:13], v[160:163], v[230:233], v[10:13]
	s_setprio 0
	s_setprio 1
	v_mfma_f32_16x16x32_bf16 v[54:57], v[164:167], v[200:203], 0
	v_mfma_f32_16x16x32_bf16 v[50:53], v[192:195], v[200:203], 0
	v_mfma_f32_16x16x32_bf16 v[38:41], v[164:167], v[208:211], 0
	v_mfma_f32_16x16x32_bf16 v[34:37], v[192:195], v[208:211], 0
	v_mfma_f32_16x16x32_bf16 v[22:25], v[164:167], v[216:219], 0
	v_mfma_f32_16x16x32_bf16 v[18:21], v[192:195], v[216:219], 0
	v_mfma_f32_16x16x32_bf16 v[6:9], v[164:167], v[224:227], 0
	v_mfma_f32_16x16x32_bf16 v[2:5], v[192:195], v[224:227], 0
	v_mfma_f32_16x16x32_bf16 v[54:57], v[182:185], v[204:207], v[54:57]
	v_mfma_f32_16x16x32_bf16 v[50:53], v[196:199], v[204:207], v[50:53]
	v_mfma_f32_16x16x32_bf16 v[38:41], v[182:185], v[212:215], v[38:41]
	v_mfma_f32_16x16x32_bf16 v[34:37], v[196:199], v[212:215], v[34:37]
	v_mfma_f32_16x16x32_bf16 v[22:25], v[182:185], v[220:223], v[22:25]
	v_mfma_f32_16x16x32_bf16 v[18:21], v[196:199], v[220:223], v[18:21]
	v_mfma_f32_16x16x32_bf16 v[6:9], v[182:185], v[230:233], v[6:9]
	v_mfma_f32_16x16x32_bf16 v[2:5], v[196:199], v[230:233], v[2:5]
	s_setprio 0
	s_barrier
	s_add_i32 s61, 0, 0x18000
	s_add_i32 s62, 0, 0x1c000
	v_add_u32_e32 v160, s61, v1
	v_add_u32_e32 v170, s62, v1
	ds_read_b128 v[130:133], v160
	ds_read_b128 v[134:137], v160 offset:1024
	ds_read_b128 v[138:141], v160 offset:2048
	ds_read_b128 v[160:163], v160 offset:3072
	ds_read_b128 v[164:167], v170
	ds_read_b128 v[182:185], v170 offset:1024
	ds_read_b128 v[192:195], v170 offset:2048
	ds_read_b128 v[196:199], v170 offset:3072
	s_add_u32 s26, s26, 0x40000
	s_addc_u32 s27, s27, 0
	s_mov_b32 m0, s31
	v_lshl_add_u64 v[236:237], s[26:27], 0, v[148:149]
	ds_read_b128 v[200:203], v189 offset:32768
	ds_read_b128 v[204:207], v189 offset:33792
	ds_read_b128 v[208:211], v189 offset:34816
	ds_read_b128 v[212:215], v189 offset:35840
	ds_read_b128 v[216:219], v189 offset:36864
	ds_read_b128 v[220:223], v189 offset:37888
	ds_read_b128 v[224:227], v189 offset:38912
	ds_read_b128 v[230:233], v189 offset:39936
	global_load_lds_dwordx4 v[236:237], off
	v_lshl_add_u64 v[236:237], s[26:27], 0, v[144:145]
	s_mov_b32 m0, s34
	s_nop 0
	global_load_lds_dwordx4 v[236:237], off
	s_waitcnt vmcnt(8)
	s_waitcnt lgkmcnt(0)
	s_barrier
	s_setprio 1
	s_waitcnt lgkmcnt(0)
	v_mfma_f32_16x16x32_bf16 v[126:129], v[130:133], v[200:203], v[126:129]
	v_mfma_f32_16x16x32_bf16 v[122:125], v[138:141], v[200:203], v[122:125]
	v_mfma_f32_16x16x32_bf16 v[110:113], v[130:133], v[208:211], v[110:113]
	v_mfma_f32_16x16x32_bf16 v[106:109], v[138:141], v[208:211], v[106:109]
	v_mfma_f32_16x16x32_bf16 v[94:97], v[130:133], v[216:219], v[94:97]
	v_mfma_f32_16x16x32_bf16 v[90:93], v[138:141], v[216:219], v[90:93]
	v_mfma_f32_16x16x32_bf16 v[78:81], v[130:133], v[224:227], v[78:81]
	v_mfma_f32_16x16x32_bf16 v[74:77], v[138:141], v[224:227], v[74:77]
	v_mfma_f32_16x16x32_bf16 v[126:129], v[134:137], v[204:207], v[126:129]
	v_mfma_f32_16x16x32_bf16 v[122:125], v[160:163], v[204:207], v[122:125]
	v_mfma_f32_16x16x32_bf16 v[110:113], v[134:137], v[212:215], v[110:113]
	v_mfma_f32_16x16x32_bf16 v[106:109], v[160:163], v[212:215], v[106:109]
	v_mfma_f32_16x16x32_bf16 v[94:97], v[134:137], v[220:223], v[94:97]
	v_mfma_f32_16x16x32_bf16 v[90:93], v[160:163], v[220:223], v[90:93]
	v_mfma_f32_16x16x32_bf16 v[78:81], v[134:137], v[230:233], v[78:81]
	v_mfma_f32_16x16x32_bf16 v[74:77], v[160:163], v[230:233], v[74:77]
	s_setprio 0
	s_setprio 1
	v_mfma_f32_16x16x32_bf16 v[118:121], v[164:167], v[200:203], v[118:121]
	v_mfma_f32_16x16x32_bf16 v[114:117], v[192:195], v[200:203], v[114:117]
	v_mfma_f32_16x16x32_bf16 v[102:105], v[164:167], v[208:211], v[102:105]
	v_mfma_f32_16x16x32_bf16 v[98:101], v[192:195], v[208:211], v[98:101]
	v_mfma_f32_16x16x32_bf16 v[86:89], v[164:167], v[216:219], v[86:89]
	v_mfma_f32_16x16x32_bf16 v[82:85], v[192:195], v[216:219], v[82:85]
	v_mfma_f32_16x16x32_bf16 v[70:73], v[164:167], v[224:227], v[70:73]
	v_mfma_f32_16x16x32_bf16 v[66:69], v[192:195], v[224:227], v[66:69]
	v_mfma_f32_16x16x32_bf16 v[118:121], v[182:185], v[204:207], v[118:121]
	v_mfma_f32_16x16x32_bf16 v[114:117], v[196:199], v[204:207], v[114:117]
	v_mfma_f32_16x16x32_bf16 v[102:105], v[182:185], v[212:215], v[102:105]
	v_mfma_f32_16x16x32_bf16 v[98:101], v[196:199], v[212:215], v[98:101]
	v_mfma_f32_16x16x32_bf16 v[86:89], v[182:185], v[220:223], v[86:89]
	v_mfma_f32_16x16x32_bf16 v[82:85], v[196:199], v[220:223], v[82:85]
	v_mfma_f32_16x16x32_bf16 v[70:73], v[182:185], v[230:233], v[70:73]
	v_mfma_f32_16x16x32_bf16 v[66:69], v[196:199], v[230:233], v[66:69]
	s_setprio 0
	s_barrier
; #define PG8_STAGE_A(b, h, ptr, NX) do { if constexpr (Sched::GATHER) { unsigned gs_[2]; gs_[0] = ((NX) && last_) ? gN[h][0] : gA[h][0]; gs_[1] = ((NX) && last_) ? gN[h][1] : gA[h][1]; PG8_STAGE(PG8_SA(b, h), ptr, gs_); } \
;         else PG8_STAGE(PG8_SA(b, h), (ptr) + ((h) ? hstep : (size_t)0), voffA); } while (0)
; #define PG8_STAGE(bufoff, gbase, voff) do { _Pragma("unroll") for (int _i = 0; _i < 2; ++_i) \
;         __builtin_amdgcn_global_load_lds((const unsigned*)((const char*)(gbase) + (voff)[_i]), (PG8_LAS unsigned*)(lds + (bufoff) + ldsw + _i * 8192), 16, 0, 0); } while (0)
; #define PG8_LDA(dst, b, h) do { _Pragma("unroll") for (int m = 0; m < 4; ++m) _Pragma("unroll") for (int k = 0; k < 2; ++k) dst[m][k] = *(const PG8_LAS bf16x8*)(lds + PG8_SA(b, h) + aoff + m * 2048 + k * 1024); } while (0)
; #define PG8_MMA(ai, bj, At, Bt) do { __builtin_amdgcn_s_setprio(1); _Pragma("unroll") for (int m = 0; m < 4; ++m) _Pragma("unroll") for (int n = 0; n < 2; ++n) _Pragma("unroll") for (int k = 0; k < 2; ++k) \
;         acc[ai][bj][m][n] = __builtin_amdgcn_mfma_f32_16x16x32_bf16(Bt[n][k], At[m][k], acc[ai][bj][m][n], 0, 0, 0); __builtin_amdgcn_s_setprio(0); } while (0)
; #define PG8_WAIT_V(n) asm volatile("s_waitcnt vmcnt(" #n ")" ::: "memory")
; #define PG8_WAIT_L(n) asm volatile("s_waitcnt lgkmcnt(" #n ")" ::: "memory")
; #define PG8_BAR __builtin_amdgcn_s_barrier()
; #define PG8_SCHED __builtin_amdgcn_sched_barrier(0)
; template <class Epi, class Sched, bool ALIGN_EPI = false, bool SP2 = false>
; __device__ __forceinline__ void gemm_phase(PG8_LAS unsigned char* lds, const Gemm g, const Sched& S, const Epi& E, const bool skip_epi = false) {
;     ...
;         for (int t = 0; t < nt; t += 2) {
;             const bool last = (t == nt - 2); last_ = last && has_next;
;             const char* a1 = cA + (size_t)(t + 1) * kstep;
;             const char* a2 = last ? nA : cA + (size_t)(t + 2) * kstep; const char* b2 = last ? nB : cB + (size_t)(t + 2) * kstep;
;     ...
;             PG8_LDA(At, 1, 1); PG8_STAGE(PG8_SB(1, 0), b3, voffB); PG8_STAGE(PG8_SB(1, 1), b3 + hstep, voffB); PG8_STAGE_A(1, 0, a3, true);
;             PG8_WAIT_V(8); PG8_WAIT_L(0); PG8_BAR; PG8_MMA(1, 0, At, B0); PG8_MMA(1, 1, At, B1); PG8_BAR; PG8_SCHED;
	s_add_i32 s26, s61, s2
	v_lshl_add_u64 v[168:169], v[168:169], 0, s[8:9]
	s_mov_b32 m0, s26
	ds_read_b128 v[200:203], v189 offset:49152
	ds_read_b128 v[204:207], v189 offset:50176
	ds_read_b128 v[208:211], v189 offset:51200
	ds_read_b128 v[212:215], v189 offset:52224
	ds_read_b128 v[216:219], v189 offset:53248
	ds_read_b128 v[220:223], v189 offset:54272
	ds_read_b128 v[224:227], v189 offset:55296
	ds_read_b128 v[230:233], v189 offset:56320
	global_load_lds_dwordx4 v[168:169], off
	s_add_i32 m0, s26, 0x2000
	s_add_u32 s24, s24, 0x40080
	v_lshl_add_u64 v[168:169], v[172:173], 0, s[8:9]
	s_addc_u32 s25, s25, 0
	s_add_i32 s26, s62, s2
	global_load_lds_dwordx4 v[168:169], off
	v_lshl_add_u64 v[168:169], s[24:25], 0, v[146:147]
	s_mov_b32 m0, s26
	s_nop 0
	global_load_lds_dwordx4 v[168:169], off
	v_lshl_add_u64 v[168:169], s[24:25], 0, v[142:143]
	s_add_i32 m0, s26, 0x2000
	s_nop 0
	global_load_lds_dwordx4 v[168:169], off
	v_lshl_add_u64 v[168:169], v[176:177], 0, s[8:9]
	s_mov_b32 m0, s36
	s_nop 0
	global_load_lds_dwordx4 v[168:169], off
	v_lshl_add_u64 v[168:169], v[234:235], 0, s[8:9]
	s_mov_b32 m0, s37
	s_nop 0
	global_load_lds_dwordx4 v[168:169], off
	s_waitcnt vmcnt(8)
	s_waitcnt lgkmcnt(0)
	s_barrier
	s_setprio 1
	s_waitcnt lgkmcnt(0)
	v_mfma_f32_16x16x32_bf16 v[62:65], v[130:133], v[200:203], v[62:65]
	v_mfma_f32_16x16x32_bf16 v[58:61], v[138:141], v[200:203], v[58:61]
	v_mfma_f32_16x16x32_bf16 v[46:49], v[130:133], v[208:211], v[46:49]
	v_mfma_f32_16x16x32_bf16 v[42:45], v[138:141], v[208:211], v[42:45]
	v_mfma_f32_16x16x32_bf16 v[30:33], v[130:133], v[216:219], v[30:33]
	v_mfma_f32_16x16x32_bf16 v[26:29], v[138:141], v[216:219], v[26:29]
	v_mfma_f32_16x16x32_bf16 v[14:17], v[130:133], v[224:227], v[14:17]
	v_mfma_f32_16x16x32_bf16 v[10:13], v[138:141], v[224:227], v[10:13]
	v_mfma_f32_16x16x32_bf16 v[62:65], v[134:137], v[204:207], v[62:65]
	v_mfma_f32_16x16x32_bf16 v[58:61], v[160:163], v[204:207], v[58:61]
	v_mfma_f32_16x16x32_bf16 v[46:49], v[134:137], v[212:215], v[46:49]
	v_mfma_f32_16x16x32_bf16 v[42:45], v[160:163], v[212:215], v[42:45]
	v_mfma_f32_16x16x32_bf16 v[30:33], v[134:137], v[220:223], v[30:33]
	v_mfma_f32_16x16x32_bf16 v[26:29], v[160:163], v[220:223], v[26:29]
	v_mfma_f32_16x16x32_bf16 v[14:17], v[134:137], v[230:233], v[14:17]
	v_mfma_f32_16x16x32_bf16 v[10:13], v[160:163], v[230:233], v[10:13]
	s_setprio 0
	s_setprio 1
	v_mfma_f32_16x16x32_bf16 v[54:57], v[164:167], v[200:203], v[54:57]
	v_mfma_f32_16x16x32_bf16 v[50:53], v[192:195], v[200:203], v[50:53]
	v_mfma_f32_16x16x32_bf16 v[38:41], v[164:167], v[208:211], v[38:41]
	v_mfma_f32_16x16x32_bf16 v[34:37], v[192:195], v[208:211], v[34:37]
	v_mfma_f32_16x16x32_bf16 v[22:25], v[164:167], v[216:219], v[22:25]
	v_mfma_f32_16x16x32_bf16 v[18:21], v[192:195], v[216:219], v[18:21]
	v_mfma_f32_16x16x32_bf16 v[6:9], v[164:167], v[224:227], v[6:9]
	v_mfma_f32_16x16x32_bf16 v[2:5], v[192:195], v[224:227], v[2:5]
	v_mfma_f32_16x16x32_bf16 v[54:57], v[182:185], v[204:207], v[54:57]
	v_mfma_f32_16x16x32_bf16 v[50:53], v[196:199], v[204:207], v[50:53]
	v_mfma_f32_16x16x32_bf16 v[38:41], v[182:185], v[212:215], v[38:41]
	v_mfma_f32_16x16x32_bf16 v[34:37], v[196:199], v[212:215], v[34:37]
	v_mfma_f32_16x16x32_bf16 v[22:25], v[182:185], v[220:223], v[22:25]
	v_mfma_f32_16x16x32_bf16 v[18:21], v[196:199], v[220:223], v[18:21]
	v_mfma_f32_16x16x32_bf16 v[6:9], v[182:185], v[230:233], v[6:9]
	v_mfma_f32_16x16x32_bf16 v[2:5], v[196:199], v[230:233], v[2:5]
	s_setprio 0
	s_barrier
	s_add_i32 s60, s60, 2
	s_add_u32 s22, s22, 0x100
	s_addc_u32 s23, s23, 0
	s_add_u32 s58, s58, 0x100
	s_addc_u32 s59, s59, 0
	s_cmp_gt_u32 s60, 13

; __device__ __forceinline__ unsigned cvt_pk_bf16(float lo, float hi) { const f32x2c_t v = {lo, hi}; return __builtin_bit_cast(unsigned, __builtin_convertvector(v, bf16x2c_t)); }
; __device__ __forceinline__ float silu_f(float a) { return a * __builtin_amdgcn_rcpf(1.0f + __builtin_amdgcn_exp2f(a * -1.4426950408889634f)); }
; __device__ __forceinline__ void rstd8(const float* SS, int rowb, int lane, float (&rs)[2][4]) {
;     ...
;         for (int m = 0; m < 4; ++m) { float s = (p[ai][m][0] + p[ai][m][1]) + (p[ai][m][2] + p[ai][m][3]); s += __shfl_xor(s, 1); s += __shfl_xor(s, 2);
;             const float r = __builtin_amdgcn_rsqf(s * (1.0f / 1024.0f) + RMS_EPS);
;             rs[ai][m] = __builtin_bit_cast(float, __builtin_amdgcn_ds_bpermute((lane & 15) << 4, __builtin_bit_cast(int, r))); }
;     __device__ __forceinline__ void operator()(const f32x4 (&acc)[2][2][4][2], const Unit& u, int wr, int wc, int fr, int fq) const {
;     ...
;         } else rstd8(SS, u.pm * BM + wr * 64, lane, rs8);
; #pragma unroll
;         for (int ai = 0; ai < 2; ++ai) {
; #pragma unroll
;             for (int m = 0; m < 4; ++m) { const int row = row0 + ai * HALF + m * 16; const float rs = rs8[ai][m];
;                 const f32x4 a0 = acc[ai][0][m][0] * rs, a1 = acc[ai][0][m][1] * rs, b0 = acc[ai][1][m][0] * rs, b1 = acc[ai][1][m][1] * rs;
;                 f32x4 g0, g1;
; #pragma unroll
;                 for (int j = 0; j < 4; ++j) { g0[j] = silu_f(a0[j]) * b0[j]; g1[j] = silu_f(a1[j]) * b1[j]; }
;                 u32x4 w; w.x = cvt_pk_bf16(g0[0], g0[1]); w.y = cvt_pk_bf16(g0[2], g0[3]); w.z = cvt_pk_bf16(g1[0], g1[1]); w.w = cvt_pk_bf16(g1[2], g1[3]);
;                 w = lane_perm(w, qs4); u32x4* dst = (u32x4*)(O + (size_t)(rowS + ai * HALF + m * 16) * ldo + colS); (void)row;
.LBB0_724:
	v_lshl_add_u32 v182, s20, 8, v175
	v_ashrrev_i32_e32 v183, 31, v182
	v_lshlrev_b64 v[130:131], 6, v[182:183]
	v_lshl_add_u64 v[130:131], v[150:151], 0, v[130:131]
	v_add_co_u32_e32 v132, vcc, 0x2000, v130
	v_addc_co_u32_e32 v133, vcc, 0, v131, vcc
	global_load_dwordx4 v[208:211], v[132:133], off
	global_load_dwordx4 v[212:215], v[132:133], off offset:1024
	global_load_dwordx4 v[216:219], v[132:133], off offset:2048
	global_load_dwordx4 v[220:223], v[132:133], off offset:3072
	v_add_f32_e32 v238, v238, v239
	v_add_f32_e32 v242, v242, v243
	v_add_f32_e32 v246, v246, v247
	v_add_f32_e32 v250, v250, v251
	v_add_f32_e32 v240, v240, v241
	v_add_f32_e32 v244, v244, v245
	v_add_f32_e32 v248, v248, v249
	v_add_f32_e32 v252, v252, v253
	v_add_f32_e32 v238, v238, v240
	v_add_f32_e32 v242, v242, v244
	v_add_f32_e32 v246, v246, v248
	v_add_f32_e32 v250, v250, v252
	v_add_f32_dpp v238, v238, v238 quad_perm:[1,0,3,2] row_mask:0xf bank_mask:0xf
	v_add_f32_dpp v242, v242, v242 quad_perm:[1,0,3,2] row_mask:0xf bank_mask:0xf
	v_add_f32_dpp v246, v246, v246 quad_perm:[1,0,3,2] row_mask:0xf bank_mask:0xf
	v_add_f32_dpp v250, v250, v250 quad_perm:[1,0,3,2] row_mask:0xf bank_mask:0xf
	v_add_f32_dpp v238, v238, v238 quad_perm:[2,3,0,1] row_mask:0xf bank_mask:0xf
	v_add_f32_dpp v242, v242, v242 quad_perm:[2,3,0,1] row_mask:0xf bank_mask:0xf
	v_add_f32_dpp v246, v246, v246 quad_perm:[2,3,0,1] row_mask:0xf bank_mask:0xf
	v_add_f32_dpp v250, v250, v250 quad_perm:[2,3,0,1] row_mask:0xf bank_mask:0xf
	v_fmamk_f32 v238, v238, 0x3a800000, v190
	v_fmamk_f32 v242, v242, 0x3a800000, v190
	v_fmamk_f32 v246, v246, 0x3a800000, v190
	v_fmamk_f32 v250, v250, 0x3a800000, v190
	ds_bpermute_b32 v238, v179, v238
	ds_bpermute_b32 v242, v179, v242
	ds_bpermute_b32 v246, v179, v246
	ds_bpermute_b32 v250, v179, v250
	v_lshl_or_b32 v184, s21, 7, v181
	v_ashrrev_i32_e32 v185, 31, v184
	v_mov_b64_e32 v[134:135], s[44:45]
	v_lshlrev_b64 v[184:185], 1, v[184:185]
	v_mad_i64_i32 v[224:225], s[20:21], v182, s49, v[134:135]
	s_nop 0
	v_lshl_add_u64 v[224:225], v[224:225], 0, v[184:185]
	v_pk_mul_f32 v[118:119], v[118:119], v[126:127]
	v_pk_mul_f32 v[120:121], v[120:121], v[128:129]
	v_pk_mul_f32 v[114:115], v[114:115], v[122:123]
	v_pk_mul_f32 v[116:117], v[116:117], v[124:125]
	v_pk_mul_f32 v[102:103], v[102:103], v[110:111]
	v_pk_mul_f32 v[104:105], v[104:105], v[112:113]
	v_pk_mul_f32 v[98:99], v[98:99], v[106:107]
	v_pk_mul_f32 v[100:101], v[100:101], v[108:109]
	v_pk_mul_f32 v[86:87], v[86:87], v[94:95]
	v_pk_mul_f32 v[88:89], v[88:89], v[96:97]
	v_pk_mul_f32 v[82:83], v[82:83], v[90:91]
	v_pk_mul_f32 v[84:85], v[84:85], v[92:93]
	v_pk_mul_f32 v[70:71], v[70:71], v[78:79]
	v_pk_mul_f32 v[72:73], v[72:73], v[80:81]
	v_pk_mul_f32 v[66:67], v[66:67], v[74:75]
	v_pk_mul_f32 v[68:69], v[68:69], v[76:77]
	v_pk_mul_f32 v[54:55], v[54:55], v[62:63]
	v_pk_mul_f32 v[56:57], v[56:57], v[64:65]
	v_pk_mul_f32 v[50:51], v[50:51], v[58:59]
	v_pk_mul_f32 v[52:53], v[52:53], v[60:61]
	v_pk_mul_f32 v[38:39], v[38:39], v[46:47]
	v_pk_mul_f32 v[40:41], v[40:41], v[48:49]
	v_pk_mul_f32 v[34:35], v[34:35], v[42:43]
	v_pk_mul_f32 v[36:37], v[36:37], v[44:45]
	v_pk_mul_f32 v[22:23], v[22:23], v[30:31]
	v_pk_mul_f32 v[24:25], v[24:25], v[32:33]
	v_pk_mul_f32 v[18:19], v[18:19], v[26:27]
	v_pk_mul_f32 v[20:21], v[20:21], v[28:29]
	v_pk_mul_f32 v[6:7], v[6:7], v[14:15]
	v_pk_mul_f32 v[8:9], v[8:9], v[16:17]
	v_pk_mul_f32 v[2:3], v[2:3], v[10:11]
	v_pk_mul_f32 v[4:5], v[4:5], v[12:13]
	s_waitcnt lgkmcnt(0)
	v_rsq_f32_e32 v240, v238
	v_rsq_f32_e32 v244, v242
	v_rsq_f32_e32 v248, v246
	v_rsq_f32_e32 v252, v250
	s_nop 0
	v_mul_f32_e32 v240, 0xbfb8aa3b, v240
	v_mul_f32_e32 v244, 0xbfb8aa3b, v244
	v_mul_f32_e32 v248, 0xbfb8aa3b, v248
	v_mul_f32_e32 v252, 0xbfb8aa3b, v252
	v_pk_mul_f32 v[126:127], v[126:127], v[240:241] op_sel_hi:[1,0]
	v_pk_mul_f32 v[128:129], v[128:129], v[240:241] op_sel_hi:[1,0]
	v_pk_mul_f32 v[122:123], v[122:123], v[240:241] op_sel_hi:[1,0]
	v_pk_mul_f32 v[124:125], v[124:125], v[240:241] op_sel_hi:[1,0]
	v_exp_f32_e32 v126, v126
	v_exp_f32_e32 v127, v127
	v_exp_f32_e32 v128, v128
	v_exp_f32_e32 v129, v129
	v_exp_f32_e32 v122, v122
	v_exp_f32_e32 v123, v123
	v_exp_f32_e32 v124, v124
	v_exp_f32_e32 v125, v125
	v_pk_fma_f32 v[126:127], v[126:127], v[238:239], v[238:239] op_sel_hi:[1,0,0]
	v_pk_fma_f32 v[128:129], v[128:129], v[238:239], v[238:239] op_sel_hi:[1,0,0]
	v_pk_fma_f32 v[122:123], v[122:123], v[238:239], v[238:239] op_sel_hi:[1,0,0]
	v_pk_fma_f32 v[124:125], v[124:125], v[238:239], v[238:239] op_sel_hi:[1,0,0]
	v_rcp_f32_e32 v126, v126
	v_rcp_f32_e32 v127, v127
	v_rcp_f32_e32 v128, v128
	v_rcp_f32_e32 v129, v129
	v_rcp_f32_e32 v122, v122
	v_rcp_f32_e32 v123, v123
	v_rcp_f32_e32 v124, v124
	v_rcp_f32_e32 v125, v125
	v_pk_mul_f32 v[118:119], v[118:119], v[126:127]
	v_pk_mul_f32 v[120:121], v[120:121], v[128:129]
	v_pk_mul_f32 v[114:115], v[114:115], v[122:123]
	v_pk_mul_f32 v[116:117], v[116:117], v[124:125]
	v_cvt_pk_bf16_f32 v126, v118, v119
	v_cvt_pk_bf16_f32 v127, v120, v121
	v_cvt_pk_bf16_f32 v128, v114, v115
	v_cvt_pk_bf16_f32 v129, v116, v117
	ds_bpermute_b32 v122, v171, v126
	ds_bpermute_b32 v123, v171, v127
	ds_bpermute_b32 v124, v171, v128
	ds_bpermute_b32 v125, v171, v129
	v_mov_b32_e32 v226, v224
	v_mov_b32_e32 v227, v225
	v_pk_mul_f32 v[110:111], v[110:111], v[244:245] op_sel_hi:[1,0]
	v_pk_mul_f32 v[112:113], v[112:113], v[244:245] op_sel_hi:[1,0]
	v_pk_mul_f32 v[106:107], v[106:107], v[244:245] op_sel_hi:[1,0]
	v_pk_mul_f32 v[108:109], v[108:109], v[244:245] op_sel_hi:[1,0]
	v_exp_f32_e32 v110, v110
	v_exp_f32_e32 v111, v111
	v_exp_f32_e32 v112, v112
	v_exp_f32_e32 v113, v113
	v_exp_f32_e32 v106, v106
	v_exp_f32_e32 v107, v107
	v_exp_f32_e32 v108, v108
	v_exp_f32_e32 v109, v109
	v_pk_fma_f32 v[110:111], v[110:111], v[242:243], v[242:243] op_sel_hi:[1,0,0]
	v_pk_fma_f32 v[112:113], v[112:113], v[242:243], v[242:243] op_sel_hi:[1,0,0]
	v_pk_fma_f32 v[106:107], v[106:107], v[242:243], v[242:243] op_sel_hi:[1,0,0]
	v_pk_fma_f32 v[108:109], v[108:109], v[242:243], v[242:243] op_sel_hi:[1,0,0]
	v_rcp_f32_e32 v110, v110
	v_rcp_f32_e32 v111, v111
	v_rcp_f32_e32 v112, v112
	v_rcp_f32_e32 v113, v113
	v_rcp_f32_e32 v106, v106
	v_rcp_f32_e32 v107, v107
	v_rcp_f32_e32 v108, v108
	v_rcp_f32_e32 v109, v109
	v_pk_mul_f32 v[102:103], v[102:103], v[110:111]
	v_pk_mul_f32 v[104:105], v[104:105], v[112:113]
	v_pk_mul_f32 v[98:99], v[98:99], v[106:107]
	v_pk_mul_f32 v[100:101], v[100:101], v[108:109]
	s_waitcnt lgkmcnt(0)
; __device__ __forceinline__ unsigned cvt_pk_bf16(float lo, float hi) { const f32x2c_t v = {lo, hi}; return __builtin_bit_cast(unsigned, __builtin_convertvector(v, bf16x2c_t)); }
; __device__ __forceinline__ float silu_f(float a) { return a * __builtin_amdgcn_rcpf(1.0f + __builtin_amdgcn_exp2f(a * -1.4426950408889634f)); }
; __device__ __forceinline__ void rstd8(const float* SS, int rowb, int lane, float (&rs)[2][4]) {
;     ...
;         for (int m = 0; m < 4; ++m) { float s = (p[ai][m][0] + p[ai][m][1]) + (p[ai][m][2] + p[ai][m][3]); s += __shfl_xor(s, 1); s += __shfl_xor(s, 2);
;             const float r = __builtin_amdgcn_rsqf(s * (1.0f / 1024.0f) + RMS_EPS);
;             rs[ai][m] = __builtin_bit_cast(float, __builtin_amdgcn_ds_bpermute((lane & 15) << 4, __builtin_bit_cast(int, r))); }
;     __device__ __forceinline__ void operator()(const f32x4 (&acc)[2][2][4][2], const Unit& u, int wr, int wc, int fr, int fq) const {
;     ...
;         for (int ai = 0; ai < 2; ++ai) {
; #pragma unroll
;             for (int m = 0; m < 4; ++m) { const int row = row0 + ai * HALF + m * 16; const float rs = rs8[ai][m];
;                 const f32x4 a0 = acc[ai][0][m][0] * rs, a1 = acc[ai][0][m][1] * rs, b0 = acc[ai][1][m][0] * rs, b1 = acc[ai][1][m][1] * rs;
;                 f32x4 g0, g1;
; #pragma unroll
;                 for (int j = 0; j < 4; ++j) { g0[j] = silu_f(a0[j]) * b0[j]; g1[j] = silu_f(a1[j]) * b1[j]; }
;                 u32x4 w; w.x = cvt_pk_bf16(g0[0], g0[1]); w.y = cvt_pk_bf16(g0[2], g0[3]); w.z = cvt_pk_bf16(g1[0], g1[1]); w.w = cvt_pk_bf16(g1[2], g1[3]);
;                 w = lane_perm(w, qs4); u32x4* dst = (u32x4*)(O + (size_t)(rowS + ai * HALF + m * 16) * ldo + colS); (void)row;
	global_store_dwordx4 v[226:227], v[122:125], off
	v_cvt_pk_bf16_f32 v110, v102, v103
	v_cvt_pk_bf16_f32 v111, v104, v105
	v_cvt_pk_bf16_f32 v112, v98, v99
	v_cvt_pk_bf16_f32 v113, v100, v101
	ds_bpermute_b32 v106, v171, v110
	ds_bpermute_b32 v107, v171, v111
	ds_bpermute_b32 v108, v171, v112
	ds_bpermute_b32 v109, v171, v113
	v_add_co_u32_e32 v230, vcc, 0x16000, v224
	v_addc_co_u32_e32 v231, vcc, 0, v225, vcc
	v_pk_mul_f32 v[94:95], v[94:95], v[248:249] op_sel_hi:[1,0]
	v_pk_mul_f32 v[96:97], v[96:97], v[248:249] op_sel_hi:[1,0]
	v_pk_mul_f32 v[90:91], v[90:91], v[248:249] op_sel_hi:[1,0]
	v_pk_mul_f32 v[92:93], v[92:93], v[248:249] op_sel_hi:[1,0]
	v_exp_f32_e32 v94, v94
	v_exp_f32_e32 v95, v95
	v_exp_f32_e32 v96, v96
	v_exp_f32_e32 v97, v97
	v_exp_f32_e32 v90, v90
	v_exp_f32_e32 v91, v91
	v_exp_f32_e32 v92, v92
	v_exp_f32_e32 v93, v93
	v_pk_fma_f32 v[94:95], v[94:95], v[246:247], v[246:247] op_sel_hi:[1,0,0]
	v_pk_fma_f32 v[96:97], v[96:97], v[246:247], v[246:247] op_sel_hi:[1,0,0]
	v_pk_fma_f32 v[90:91], v[90:91], v[246:247], v[246:247] op_sel_hi:[1,0,0]
	v_pk_fma_f32 v[92:93], v[92:93], v[246:247], v[246:247] op_sel_hi:[1,0,0]
	v_rcp_f32_e32 v94, v94
	v_rcp_f32_e32 v95, v95
	v_rcp_f32_e32 v96, v96
	v_rcp_f32_e32 v97, v97
	v_rcp_f32_e32 v90, v90
	v_rcp_f32_e32 v91, v91
	v_rcp_f32_e32 v92, v92
	v_rcp_f32_e32 v93, v93
	v_pk_mul_f32 v[86:87], v[86:87], v[94:95]
	v_pk_mul_f32 v[88:89], v[88:89], v[96:97]
	v_pk_mul_f32 v[82:83], v[82:83], v[90:91]
	v_pk_mul_f32 v[84:85], v[84:85], v[92:93]
	s_waitcnt lgkmcnt(0)
	global_store_dwordx4 v[230:231], v[106:109], off
	v_cvt_pk_bf16_f32 v94, v86, v87
	v_cvt_pk_bf16_f32 v95, v88, v89
	v_cvt_pk_bf16_f32 v96, v82, v83
	v_cvt_pk_bf16_f32 v97, v84, v85
	ds_bpermute_b32 v90, v171, v94
	ds_bpermute_b32 v91, v171, v95
	ds_bpermute_b32 v92, v171, v96
	ds_bpermute_b32 v93, v171, v97
	v_add_co_u32_e32 v226, vcc, 0x2c000, v224
	v_addc_co_u32_e32 v227, vcc, 0, v225, vcc
	v_pk_mul_f32 v[78:79], v[78:79], v[252:253] op_sel_hi:[1,0]
	v_pk_mul_f32 v[80:81], v[80:81], v[252:253] op_sel_hi:[1,0]
	v_pk_mul_f32 v[74:75], v[74:75], v[252:253] op_sel_hi:[1,0]
	v_pk_mul_f32 v[76:77], v[76:77], v[252:253] op_sel_hi:[1,0]
	v_exp_f32_e32 v78, v78
	v_exp_f32_e32 v79, v79
	v_exp_f32_e32 v80, v80
	v_exp_f32_e32 v81, v81
	v_exp_f32_e32 v74, v74
	v_exp_f32_e32 v75, v75
	v_exp_f32_e32 v76, v76
	v_exp_f32_e32 v77, v77
	v_pk_fma_f32 v[78:79], v[78:79], v[250:251], v[250:251] op_sel_hi:[1,0,0]
	v_pk_fma_f32 v[80:81], v[80:81], v[250:251], v[250:251] op_sel_hi:[1,0,0]
	v_pk_fma_f32 v[74:75], v[74:75], v[250:251], v[250:251] op_sel_hi:[1,0,0]
	v_pk_fma_f32 v[76:77], v[76:77], v[250:251], v[250:251] op_sel_hi:[1,0,0]
	v_rcp_f32_e32 v78, v78
	v_rcp_f32_e32 v79, v79
	v_rcp_f32_e32 v80, v80
	v_rcp_f32_e32 v81, v81
	v_rcp_f32_e32 v74, v74
	v_rcp_f32_e32 v75, v75
	v_rcp_f32_e32 v76, v76
	v_rcp_f32_e32 v77, v77
	v_pk_mul_f32 v[70:71], v[70:71], v[78:79]
	v_pk_mul_f32 v[72:73], v[72:73], v[80:81]
	v_pk_mul_f32 v[66:67], v[66:67], v[74:75]
	v_pk_mul_f32 v[68:69], v[68:69], v[76:77]
	s_waitcnt lgkmcnt(0)
	global_store_dwordx4 v[226:227], v[90:93], off
	v_cvt_pk_bf16_f32 v78, v70, v71
	v_cvt_pk_bf16_f32 v79, v72, v73
	v_cvt_pk_bf16_f32 v80, v66, v67
	v_cvt_pk_bf16_f32 v81, v68, v69
	ds_bpermute_b32 v74, v171, v78
	ds_bpermute_b32 v75, v171, v79
	ds_bpermute_b32 v76, v171, v80
	ds_bpermute_b32 v77, v171, v81
	v_add_co_u32_e32 v230, vcc, 0x42000, v224
	v_addc_co_u32_e32 v231, vcc, 0, v225, vcc
	s_waitcnt vmcnt(3)
	v_add_f32_e32 v208, v208, v209
	v_add_f32_e32 v212, v212, v213
	v_add_f32_e32 v216, v216, v217
	v_add_f32_e32 v220, v220, v221
	v_add_f32_e32 v210, v210, v211
	v_add_f32_e32 v214, v214, v215
	v_add_f32_e32 v218, v218, v219
	v_add_f32_e32 v222, v222, v223
	v_add_f32_e32 v208, v208, v210
	v_add_f32_e32 v212, v212, v214
	v_add_f32_e32 v216, v216, v218
	v_add_f32_e32 v220, v220, v222
	v_add_f32_dpp v208, v208, v208 quad_perm:[1,0,3,2] row_mask:0xf bank_mask:0xf
	v_add_f32_dpp v212, v212, v212 quad_perm:[1,0,3,2] row_mask:0xf bank_mask:0xf
	v_add_f32_dpp v216, v216, v216 quad_perm:[1,0,3,2] row_mask:0xf bank_mask:0xf
	v_add_f32_dpp v220, v220, v220 quad_perm:[1,0,3,2] row_mask:0xf bank_mask:0xf
	v_add_f32_dpp v208, v208, v208 quad_perm:[2,3,0,1] row_mask:0xf bank_mask:0xf
	v_add_f32_dpp v212, v212, v212 quad_perm:[2,3,0,1] row_mask:0xf bank_mask:0xf
	v_add_f32_dpp v216, v216, v216 quad_perm:[2,3,0,1] row_mask:0xf bank_mask:0xf
	v_add_f32_dpp v220, v220, v220 quad_perm:[2,3,0,1] row_mask:0xf bank_mask:0xf
	v_fmamk_f32 v208, v208, 0x3a800000, v190
	v_fmamk_f32 v212, v212, 0x3a800000, v190
	v_fmamk_f32 v216, v216, 0x3a800000, v190
	v_fmamk_f32 v220, v220, 0x3a800000, v190
	ds_bpermute_b32 v208, v179, v208
	ds_bpermute_b32 v212, v179, v212
	ds_bpermute_b32 v216, v179, v216
	ds_bpermute_b32 v220, v179, v220
	s_waitcnt lgkmcnt(0)
; __device__ __forceinline__ unsigned cvt_pk_bf16(float lo, float hi) { const f32x2c_t v = {lo, hi}; return __builtin_bit_cast(unsigned, __builtin_convertvector(v, bf16x2c_t)); }
; __device__ __forceinline__ float silu_f(float a) { return a * __builtin_amdgcn_rcpf(1.0f + __builtin_amdgcn_exp2f(a * -1.4426950408889634f)); }
;     __device__ __forceinline__ void operator()(const f32x4 (&acc)[2][2][4][2], const Unit& u, int wr, int wc, int fr, int fq) const {
;     ...
;         for (int ai = 0; ai < 2; ++ai) {
; #pragma unroll
;             for (int m = 0; m < 4; ++m) { const int row = row0 + ai * HALF + m * 16; const float rs = rs8[ai][m];
;                 const f32x4 a0 = acc[ai][0][m][0] * rs, a1 = acc[ai][0][m][1] * rs, b0 = acc[ai][1][m][0] * rs, b1 = acc[ai][1][m][1] * rs;
;                 f32x4 g0, g1;
; #pragma unroll
;                 for (int j = 0; j < 4; ++j) { g0[j] = silu_f(a0[j]) * b0[j]; g1[j] = silu_f(a1[j]) * b1[j]; }
;                 u32x4 w; w.x = cvt_pk_bf16(g0[0], g0[1]); w.y = cvt_pk_bf16(g0[2], g0[3]); w.z = cvt_pk_bf16(g1[0], g1[1]); w.w = cvt_pk_bf16(g1[2], g1[3]);
;                 w = lane_perm(w, qs4); u32x4* dst = (u32x4*)(O + (size_t)(rowS + ai * HALF + m * 16) * ldo + colS); (void)row;
;                 if constexpr (MOE) __builtin_nontemporal_store(w, dst); else *dst = w; } }
	global_store_dwordx4 v[230:231], v[74:77], off
	v_rsq_f32_e32 v210, v208
	v_rsq_f32_e32 v214, v212
	v_rsq_f32_e32 v218, v216
	v_rsq_f32_e32 v222, v220
	s_nop 0
	v_mul_f32_e32 v210, 0xbfb8aa3b, v210
	v_mul_f32_e32 v214, 0xbfb8aa3b, v214
	v_mul_f32_e32 v218, 0xbfb8aa3b, v218
	v_mul_f32_e32 v222, 0xbfb8aa3b, v222
	v_pk_mul_f32 v[62:63], v[62:63], v[210:211] op_sel_hi:[1,0]
	v_pk_mul_f32 v[64:65], v[64:65], v[210:211] op_sel_hi:[1,0]
	v_pk_mul_f32 v[58:59], v[58:59], v[210:211] op_sel_hi:[1,0]
	v_pk_mul_f32 v[60:61], v[60:61], v[210:211] op_sel_hi:[1,0]
	v_exp_f32_e32 v62, v62
	v_exp_f32_e32 v63, v63
	v_exp_f32_e32 v64, v64
	v_exp_f32_e32 v65, v65
	v_exp_f32_e32 v58, v58
	v_exp_f32_e32 v59, v59
	v_exp_f32_e32 v60, v60
	v_exp_f32_e32 v61, v61
	v_pk_fma_f32 v[62:63], v[62:63], v[208:209], v[208:209] op_sel_hi:[1,0,0]
	v_pk_fma_f32 v[64:65], v[64:65], v[208:209], v[208:209] op_sel_hi:[1,0,0]
	v_pk_fma_f32 v[58:59], v[58:59], v[208:209], v[208:209] op_sel_hi:[1,0,0]
	v_pk_fma_f32 v[60:61], v[60:61], v[208:209], v[208:209] op_sel_hi:[1,0,0]
	v_rcp_f32_e32 v62, v62
	v_rcp_f32_e32 v63, v63
	v_rcp_f32_e32 v64, v64
	v_rcp_f32_e32 v65, v65
	v_rcp_f32_e32 v58, v58
	v_rcp_f32_e32 v59, v59
	v_rcp_f32_e32 v60, v60
	v_rcp_f32_e32 v61, v61
	v_pk_mul_f32 v[54:55], v[54:55], v[62:63]
	v_pk_mul_f32 v[56:57], v[56:57], v[64:65]
	v_pk_mul_f32 v[50:51], v[50:51], v[58:59]
	v_pk_mul_f32 v[52:53], v[52:53], v[60:61]
	v_cvt_pk_bf16_f32 v62, v54, v55
	v_cvt_pk_bf16_f32 v63, v56, v57
	v_cvt_pk_bf16_f32 v64, v50, v51
	v_cvt_pk_bf16_f32 v65, v52, v53
	ds_bpermute_b32 v58, v171, v62
	ds_bpermute_b32 v59, v171, v63
	ds_bpermute_b32 v60, v171, v64
	ds_bpermute_b32 v61, v171, v65
	v_add_co_u32_e32 v226, vcc, 0xb0000, v224
	v_addc_co_u32_e32 v227, vcc, 0, v225, vcc
	v_pk_mul_f32 v[46:47], v[46:47], v[214:215] op_sel_hi:[1,0]
	v_pk_mul_f32 v[48:49], v[48:49], v[214:215] op_sel_hi:[1,0]
	v_pk_mul_f32 v[42:43], v[42:43], v[214:215] op_sel_hi:[1,0]
	v_pk_mul_f32 v[44:45], v[44:45], v[214:215] op_sel_hi:[1,0]
	v_exp_f32_e32 v46, v46
	v_exp_f32_e32 v47, v47
	v_exp_f32_e32 v48, v48
	v_exp_f32_e32 v49, v49
	v_exp_f32_e32 v42, v42
	v_exp_f32_e32 v43, v43
	v_exp_f32_e32 v44, v44
	v_exp_f32_e32 v45, v45
	v_pk_fma_f32 v[46:47], v[46:47], v[212:213], v[212:213] op_sel_hi:[1,0,0]
	v_pk_fma_f32 v[48:49], v[48:49], v[212:213], v[212:213] op_sel_hi:[1,0,0]
	v_pk_fma_f32 v[42:43], v[42:43], v[212:213], v[212:213] op_sel_hi:[1,0,0]
	v_pk_fma_f32 v[44:45], v[44:45], v[212:213], v[212:213] op_sel_hi:[1,0,0]
	v_rcp_f32_e32 v46, v46
	v_rcp_f32_e32 v47, v47
	v_rcp_f32_e32 v48, v48
	v_rcp_f32_e32 v49, v49
	v_rcp_f32_e32 v42, v42
	v_rcp_f32_e32 v43, v43
	v_rcp_f32_e32 v44, v44
	v_rcp_f32_e32 v45, v45
	v_pk_mul_f32 v[38:39], v[38:39], v[46:47]
	v_pk_mul_f32 v[40:41], v[40:41], v[48:49]
	v_pk_mul_f32 v[34:35], v[34:35], v[42:43]
	v_pk_mul_f32 v[36:37], v[36:37], v[44:45]
	s_waitcnt lgkmcnt(0)
	global_store_dwordx4 v[226:227], v[58:61], off
	v_cvt_pk_bf16_f32 v46, v38, v39
	v_cvt_pk_bf16_f32 v47, v40, v41
	v_cvt_pk_bf16_f32 v48, v34, v35
	v_cvt_pk_bf16_f32 v49, v36, v37
	ds_bpermute_b32 v42, v171, v46
	ds_bpermute_b32 v43, v171, v47
	ds_bpermute_b32 v44, v171, v48
	ds_bpermute_b32 v45, v171, v49
	v_add_co_u32_e32 v230, vcc, 0xc6000, v224
	v_addc_co_u32_e32 v231, vcc, 0, v225, vcc
	v_pk_mul_f32 v[30:31], v[30:31], v[218:219] op_sel_hi:[1,0]
	v_pk_mul_f32 v[32:33], v[32:33], v[218:219] op_sel_hi:[1,0]
	v_pk_mul_f32 v[26:27], v[26:27], v[218:219] op_sel_hi:[1,0]
	v_pk_mul_f32 v[28:29], v[28:29], v[218:219] op_sel_hi:[1,0]
	v_exp_f32_e32 v30, v30
	v_exp_f32_e32 v31, v31
	v_exp_f32_e32 v32, v32
	v_exp_f32_e32 v33, v33
	v_exp_f32_e32 v26, v26
	v_exp_f32_e32 v27, v27
	v_exp_f32_e32 v28, v28
	v_exp_f32_e32 v29, v29
	v_pk_fma_f32 v[30:31], v[30:31], v[216:217], v[216:217] op_sel_hi:[1,0,0]
	v_pk_fma_f32 v[32:33], v[32:33], v[216:217], v[216:217] op_sel_hi:[1,0,0]
	v_pk_fma_f32 v[26:27], v[26:27], v[216:217], v[216:217] op_sel_hi:[1,0,0]
	v_pk_fma_f32 v[28:29], v[28:29], v[216:217], v[216:217] op_sel_hi:[1,0,0]
	v_rcp_f32_e32 v30, v30
	v_rcp_f32_e32 v31, v31
	v_rcp_f32_e32 v32, v32
	v_rcp_f32_e32 v33, v33
	v_rcp_f32_e32 v26, v26
	v_rcp_f32_e32 v27, v27
	v_rcp_f32_e32 v28, v28
	v_rcp_f32_e32 v29, v29
	v_pk_mul_f32 v[22:23], v[22:23], v[30:31]
	v_pk_mul_f32 v[24:25], v[24:25], v[32:33]
	v_pk_mul_f32 v[18:19], v[18:19], v[26:27]
	v_pk_mul_f32 v[20:21], v[20:21], v[28:29]
	s_waitcnt lgkmcnt(0)
	global_store_dwordx4 v[230:231], v[42:45], off
	v_cvt_pk_bf16_f32 v30, v22, v23
	v_cvt_pk_bf16_f32 v31, v24, v25
	v_cvt_pk_bf16_f32 v32, v18, v19
	v_cvt_pk_bf16_f32 v33, v20, v21
	ds_bpermute_b32 v26, v171, v30
	ds_bpermute_b32 v27, v171, v31
	ds_bpermute_b32 v28, v171, v32
	ds_bpermute_b32 v29, v171, v33
	v_add_co_u32_e32 v226, vcc, 0xdc000, v224
	v_addc_co_u32_e32 v227, vcc, 0, v225, vcc
	v_pk_mul_f32 v[14:15], v[14:15], v[222:223] op_sel_hi:[1,0]
	v_pk_mul_f32 v[16:17], v[16:17], v[222:223] op_sel_hi:[1,0]
	v_pk_mul_f32 v[10:11], v[10:11], v[222:223] op_sel_hi:[1,0]
	v_pk_mul_f32 v[12:13], v[12:13], v[222:223] op_sel_hi:[1,0]
	v_exp_f32_e32 v14, v14
	v_exp_f32_e32 v15, v15
	v_exp_f32_e32 v16, v16
	v_exp_f32_e32 v17, v17
	v_exp_f32_e32 v10, v10
	v_exp_f32_e32 v11, v11
	v_exp_f32_e32 v12, v12
	v_exp_f32_e32 v13, v13
	v_pk_fma_f32 v[14:15], v[14:15], v[220:221], v[220:221] op_sel_hi:[1,0,0]
	v_pk_fma_f32 v[16:17], v[16:17], v[220:221], v[220:221] op_sel_hi:[1,0,0]
	v_pk_fma_f32 v[10:11], v[10:11], v[220:221], v[220:221] op_sel_hi:[1,0,0]
	v_pk_fma_f32 v[12:13], v[12:13], v[220:221], v[220:221] op_sel_hi:[1,0,0]
	v_rcp_f32_e32 v14, v14
	v_rcp_f32_e32 v15, v15
	v_rcp_f32_e32 v16, v16
	v_rcp_f32_e32 v17, v17
	v_rcp_f32_e32 v10, v10
	v_rcp_f32_e32 v11, v11
	v_rcp_f32_e32 v12, v12
	v_rcp_f32_e32 v13, v13
	v_pk_mul_f32 v[6:7], v[6:7], v[14:15]
	v_pk_mul_f32 v[8:9], v[8:9], v[16:17]
	v_pk_mul_f32 v[2:3], v[2:3], v[10:11]
	v_pk_mul_f32 v[4:5], v[4:5], v[12:13]
	s_waitcnt lgkmcnt(0)
	global_store_dwordx4 v[226:227], v[26:29], off
	v_cvt_pk_bf16_f32 v14, v6, v7
	v_cvt_pk_bf16_f32 v15, v8, v9
	v_cvt_pk_bf16_f32 v16, v2, v3
	v_cvt_pk_bf16_f32 v17, v4, v5
	ds_bpermute_b32 v10, v171, v14
	ds_bpermute_b32 v11, v171, v15
	ds_bpermute_b32 v12, v171, v16
	ds_bpermute_b32 v13, v171, v17
	v_add_co_u32_e32 v230, vcc, 0xf2000, v224
	v_addc_co_u32_e32 v231, vcc, 0, v225, vcc
	s_waitcnt lgkmcnt(0)
	global_store_dwordx4 v[230:231], v[10:13], off
	s_andn2_b64 vcc, exec, s[4:5]
	s_mov_b64 s[20:21], -1
	s_cbranch_vccnz .LBB0_717
	s_andn2_b64 vcc, exec, s[6:7]
	s_cbranch_vccnz .LBB0_716
	s_barrier
	s_branch .LBB0_716
